# grid barrier: XCD leaders no longer publish/wait on the per-XCD generation word (nobody polls it since members poll the global generation); removes one atomic round trip from the leaders' exit path
# speedup vs baseline: 1.0065x; 1.0044x over previous
.LBB0_156:
	s_or_b64 exec, exec, s[4:5]
	s_mov_b64 s[4:5], exec
	v_mbcnt_lo_u32_b32 v1, s4, 0
	v_mbcnt_hi_u32_b32 v1, s5, v1
	s_mov_b32 s9, 0
	v_cmp_eq_u32_e32 vcc, 0, v1
	s_waitcnt vmcnt(0)
	buffer_inv sc1
	s_and_saveexec_b64 s[6:7], vcc
	s_cbranch_execz .LBB0_158
	s_add_i32 s8, s3, 0x900
	s_lshl_b64 s[8:9], s[8:9], 2
	s_add_u32 s8, s54, s8
	s_addc_u32 s9, s55, s9
	s_bcnt1_i32_b64 s3, s[4:5]
	v_mov_b32_e32 v1, 0
	v_mov_b32_e32 v2, s3
.LBB0_158:
	s_or_b64 exec, exec, s[6:7]
	s_waitcnt vmcnt(0)

.LBB0_255:
	s_or_b64 exec, exec, s[4:5]
	s_mov_b64 s[4:5], exec
	v_mbcnt_lo_u32_b32 v2, s4, 0
	v_mbcnt_hi_u32_b32 v2, s5, v2
	v_cmp_eq_u32_e32 vcc, 0, v2
	s_waitcnt vmcnt(0)
	buffer_inv sc1
	s_and_saveexec_b64 s[6:7], vcc
	s_cbranch_execz .LBB0_257
	s_add_i32 s8, s20, 0x900
	s_mov_b32 s9, s56
	s_lshl_b64 s[8:9], s[8:9], 2
	s_add_u32 s8, s54, s8
	s_addc_u32 s9, s55, s9
	s_bcnt1_i32_b64 s4, s[4:5]
	v_mov_b32_e32 v2, s4
.LBB0_257:
	s_or_b64 exec, exec, s[6:7]
	s_waitcnt vmcnt(0)

.LBB0_322:
	s_or_b64 exec, exec, s[4:5]
	s_mov_b64 s[4:5], exec
	v_mbcnt_lo_u32_b32 v2, s4, 0
	v_mbcnt_hi_u32_b32 v2, s5, v2
	v_cmp_eq_u32_e32 vcc, 0, v2
	s_waitcnt vmcnt(0)
	buffer_inv sc1
	s_and_saveexec_b64 s[6:7], vcc
	s_cbranch_execz .LBB0_324
	s_add_i32 s8, s20, 0x900
	s_mov_b32 s9, s56
	s_lshl_b64 s[8:9], s[8:9], 2
	s_add_u32 s8, s54, s8
	s_addc_u32 s9, s55, s9
	s_bcnt1_i32_b64 s4, s[4:5]
	v_mov_b32_e32 v2, s4
.LBB0_324:
	s_or_b64 exec, exec, s[6:7]
	s_waitcnt vmcnt(0)

.LBB0_416:
	s_or_b64 exec, exec, s[4:5]
	s_mov_b64 s[4:5], exec
	v_mbcnt_lo_u32_b32 v2, s4, 0
	v_mbcnt_hi_u32_b32 v2, s5, v2
	v_cmp_eq_u32_e32 vcc, 0, v2
	s_waitcnt vmcnt(0)
	buffer_inv sc1
	s_and_saveexec_b64 s[6:7], vcc
	s_cbranch_execz .LBB0_418
	s_add_i32 s8, s20, 0x900
	s_mov_b32 s9, s56
	s_lshl_b64 s[8:9], s[8:9], 2
	s_add_u32 s8, s54, s8
	s_addc_u32 s9, s55, s9
	s_bcnt1_i32_b64 s4, s[4:5]
	v_mov_b32_e32 v2, s4
.LBB0_418:
	s_or_b64 exec, exec, s[6:7]
	s_waitcnt vmcnt(0)

.LBB0_497:
	s_or_b64 exec, exec, s[4:5]
	s_mov_b64 s[4:5], exec
	v_mbcnt_lo_u32_b32 v2, s4, 0
	v_mbcnt_hi_u32_b32 v2, s5, v2
	v_cmp_eq_u32_e32 vcc, 0, v2
	s_waitcnt vmcnt(0)
	buffer_inv sc1
	s_and_saveexec_b64 s[6:7], vcc
	s_cbranch_execz .LBB0_499
	s_add_i32 s8, s20, 0x900
	s_mov_b32 s9, s56
	s_lshl_b64 s[8:9], s[8:9], 2
	s_add_u32 s8, s54, s8
	s_addc_u32 s9, s55, s9
	s_bcnt1_i32_b64 s4, s[4:5]
	v_mov_b32_e32 v2, s4
.LBB0_499:
	s_or_b64 exec, exec, s[6:7]
	s_waitcnt vmcnt(0)

.LBB0_562:
	s_or_b64 exec, exec, s[4:5]
	s_mov_b64 s[4:5], exec
	v_mbcnt_lo_u32_b32 v2, s4, 0
	v_mbcnt_hi_u32_b32 v2, s5, v2
	v_cmp_eq_u32_e32 vcc, 0, v2
	s_waitcnt vmcnt(0)
	buffer_inv sc1
	s_and_saveexec_b64 s[6:7], vcc
	s_cbranch_execz .LBB0_564
	s_add_i32 s8, s20, 0x900
	s_mov_b32 s9, s56
	s_lshl_b64 s[8:9], s[8:9], 2
	s_add_u32 s8, s54, s8
	s_addc_u32 s9, s55, s9
	s_bcnt1_i32_b64 s4, s[4:5]
	v_mov_b32_e32 v2, s4
.LBB0_564:
	s_or_b64 exec, exec, s[6:7]
	s_waitcnt vmcnt(0)

.LBB0_893:
	s_or_b64 exec, exec, s[4:5]
	s_mov_b64 s[4:5], exec
	v_mbcnt_lo_u32_b32 v2, s4, 0
	v_mbcnt_hi_u32_b32 v2, s5, v2
	v_cmp_eq_u32_e32 vcc, 0, v2
	s_waitcnt vmcnt(0)
	buffer_inv sc1
	s_and_saveexec_b64 s[6:7], vcc
	s_cbranch_execz .LBB0_895
	s_add_i32 s8, s20, 0x900
	s_mov_b32 s9, s56
	s_lshl_b64 s[8:9], s[8:9], 2
	s_add_u32 s8, s54, s8
	s_addc_u32 s9, s55, s9
	s_bcnt1_i32_b64 s4, s[4:5]
	v_mov_b32_e32 v2, s4
.LBB0_895:
	s_or_b64 exec, exec, s[6:7]
	s_waitcnt vmcnt(0)

.LBB0_975:
	s_or_b64 exec, exec, s[4:5]
	s_mov_b64 s[4:5], exec
	v_mbcnt_lo_u32_b32 v2, s4, 0
	v_mbcnt_hi_u32_b32 v2, s5, v2
	v_cmp_eq_u32_e32 vcc, 0, v2
	s_waitcnt vmcnt(0)
	buffer_inv sc1
	s_and_saveexec_b64 s[6:7], vcc
	s_cbranch_execz .LBB0_977
	s_add_i32 s8, s20, 0x900
	s_mov_b32 s9, s56
	s_lshl_b64 s[8:9], s[8:9], 2
	s_add_u32 s8, s54, s8
	s_addc_u32 s9, s55, s9
	s_bcnt1_i32_b64 s4, s[4:5]
	v_mov_b32_e32 v2, s4
.LBB0_977:
	s_or_b64 exec, exec, s[6:7]
	s_waitcnt vmcnt(0)

.LBB0_1044:
	s_or_b64 exec, exec, s[4:5]
	s_mov_b64 s[4:5], exec
	v_mbcnt_lo_u32_b32 v2, s4, 0
	v_mbcnt_hi_u32_b32 v2, s5, v2
	v_cmp_eq_u32_e32 vcc, 0, v2
	s_waitcnt vmcnt(0)
	buffer_inv sc1
	s_and_saveexec_b64 s[6:7], vcc
	s_cbranch_execz .LBB0_1046
	s_add_i32 s8, s20, 0x900
	s_mov_b32 s9, s56
	s_lshl_b64 s[8:9], s[8:9], 2
	s_add_u32 s8, s54, s8
	s_addc_u32 s9, s55, s9
	s_bcnt1_i32_b64 s4, s[4:5]
	v_mov_b32_e32 v2, s4
.LBB0_1046:
	s_or_b64 exec, exec, s[6:7]
	s_waitcnt vmcnt(0)

.LBB0_1106:
	s_or_b64 exec, exec, s[4:5]
	s_mov_b64 s[4:5], exec
	v_mbcnt_lo_u32_b32 v2, s4, 0
	v_mbcnt_hi_u32_b32 v2, s5, v2
	v_cmp_eq_u32_e32 vcc, 0, v2
	s_waitcnt vmcnt(0)
	buffer_inv sc1
	s_and_saveexec_b64 s[6:7], vcc
	s_cbranch_execz .LBB0_1108
	s_add_i32 s8, s20, 0x900
	s_mov_b32 s9, s56
	s_lshl_b64 s[8:9], s[8:9], 2
	s_add_u32 s8, s54, s8
	s_addc_u32 s9, s55, s9
	s_bcnt1_i32_b64 s4, s[4:5]
	v_mov_b32_e32 v2, s4
.LBB0_1108:
	s_or_b64 exec, exec, s[6:7]
	s_waitcnt vmcnt(0)

.LBB0_1219:
	s_or_b64 exec, exec, s[4:5]
	s_mov_b64 s[4:5], exec
	v_mbcnt_lo_u32_b32 v2, s4, 0
	v_mbcnt_hi_u32_b32 v2, s5, v2
	v_cmp_eq_u32_e32 vcc, 0, v2
	s_waitcnt vmcnt(0)
	buffer_inv sc1
	s_and_saveexec_b64 s[6:7], vcc
	s_cbranch_execz .LBB0_1221
	s_add_i32 s8, s20, 0x900
	s_mov_b32 s9, s56
	s_lshl_b64 s[8:9], s[8:9], 2
	s_add_u32 s8, s54, s8
	s_addc_u32 s9, s55, s9
	s_bcnt1_i32_b64 s4, s[4:5]
	v_mov_b32_e32 v2, s4
.LBB0_1221:
	s_or_b64 exec, exec, s[6:7]
	s_waitcnt vmcnt(0)

.LBB0_1304:
	s_or_b64 exec, exec, s[4:5]
	s_mov_b64 s[4:5], exec
	v_mbcnt_lo_u32_b32 v2, s4, 0
	v_mbcnt_hi_u32_b32 v2, s5, v2
	v_cmp_eq_u32_e32 vcc, 0, v2
	s_waitcnt vmcnt(0)
	buffer_inv sc1
	s_and_saveexec_b64 s[6:7], vcc
	s_cbranch_execz .LBB0_1306
	s_add_i32 s8, s20, 0x900
	s_mov_b32 s9, s56
	s_lshl_b64 s[8:9], s[8:9], 2
	s_add_u32 s8, s54, s8
	s_addc_u32 s9, s55, s9
	s_bcnt1_i32_b64 s4, s[4:5]
	v_mov_b32_e32 v2, s4
.LBB0_1306:
	s_or_b64 exec, exec, s[6:7]
	s_waitcnt vmcnt(0)

.LBB0_1382:
	s_add_i32 s8, s20, 0x900
	s_mov_b32 s9, s56
	s_lshl_b64 s[8:9], s[8:9], 2
	s_add_u32 s8, s54, s8
	s_addc_u32 s9, s55, s9
	s_bcnt1_i32_b64 s4, s[4:5]
	v_mov_b32_e32 v2, s4
	s_getpc_b64 s[98:99]
